# baseline (speedup 1.0000x reference)
.Llate_block:
.Llate_end:
	s_endpgm

_Z10giou_finalPK15HIP_vector_typeIfLj2EEPf:
	s_load_dwordx2 s[2:3], s[0:1], 0x0
	v_lshlrev_b32_e32 v1, 4, v0
	v_cmp_eq_u32_e32 vcc, 0, v0
	s_waitcnt lgkmcnt(0)
	global_load_dwordx4 v[2:5], v1, s[2:3]
	global_load_dwordx4 v[6:9], v1, s[2:3] offset:1024
	s_waitcnt vmcnt(1)
	v_add_f32_e32 v1, v2, v4
	v_add_f32_e32 v2, v3, v5
	s_waitcnt vmcnt(0)
	v_add_f32_e32 v3, v6, v8
	v_add_f32_e32 v4, v7, v9
	v_add_f32_e32 v1, v1, v3
	v_add_f32_e32 v2, v2, v4
	s_nop 0
	v_add_f32_dpp v1, v1, v1 quad_perm:[1,0,3,2] row_mask:0xf bank_mask:0xf bound_ctrl:1
	v_add_f32_dpp v2, v2, v2 quad_perm:[1,0,3,2] row_mask:0xf bank_mask:0xf bound_ctrl:1
	s_nop 0
	v_add_f32_dpp v1, v1, v1 quad_perm:[2,3,0,1] row_mask:0xf bank_mask:0xf bound_ctrl:1
	v_add_f32_dpp v2, v2, v2 quad_perm:[2,3,0,1] row_mask:0xf bank_mask:0xf bound_ctrl:1
	s_nop 0
	v_add_f32_dpp v1, v1, v1 row_half_mirror row_mask:0xf bank_mask:0xf bound_ctrl:1
	v_add_f32_dpp v2, v2, v2 row_half_mirror row_mask:0xf bank_mask:0xf bound_ctrl:1
	s_nop 0
	v_add_f32_dpp v1, v1, v1 row_mirror row_mask:0xf bank_mask:0xf bound_ctrl:1
	v_add_f32_dpp v2, v2, v2 row_mirror row_mask:0xf bank_mask:0xf bound_ctrl:1
	v_readlane_b32 s2, v1, 0
	v_readlane_b32 s5, v1, 16
	v_readlane_b32 s3, v1, 32
	v_readlane_b32 s4, v1, 48
	v_readlane_b32 s6, v2, 0
	v_readlane_b32 s9, v2, 16
	v_readlane_b32 s7, v2, 32
	v_readlane_b32 s8, v2, 48
	s_and_saveexec_b64 s[10:11], vcc
	s_cbranch_execz .LBB1_2
	v_mov_b32_e32 v0, s9
	v_add_f32_e32 v0, s6, v0
	v_mov_b32_e32 v1, s5
	v_add_f32_e32 v0, s7, v0
	v_add_f32_e32 v1, s2, v1
	v_add_f32_e32 v0, s8, v0
	v_add_f32_e32 v1, s3, v1
	v_add_f32_e32 v1, s4, v1
	v_max_f32_e32 v0, 1.0, v0
	v_div_scale_f32 v2, s[2:3], v0, v0, v1
	v_rcp_f32_e32 v3, v2
	s_load_dwordx2 s[0:1], s[0:1], 0x8
	v_fma_f32 v4, -v2, v3, 1.0
	v_fmac_f32_e32 v3, v4, v3
	v_div_scale_f32 v4, vcc, v1, v0, v1
	v_mul_f32_e32 v5, v4, v3
	v_fma_f32 v6, -v2, v5, v4
	v_fmac_f32_e32 v5, v6, v3
	v_fma_f32 v2, -v2, v5, v4
	v_div_fmas_f32 v2, v2, v3, v5
	v_div_fixup_f32 v0, v2, v0, v1
	v_mov_b32_e32 v1, 0
	s_waitcnt lgkmcnt(0)
	global_store_dword v1, v0, s[0:1]
